# DSA scoring weighted sums via v_pk_mul_f32/v_pk_fma_f32 (f32 packed, 5->3 ops per 4-product group)
# baseline (speedup 1.0000x reference)
.LBB0_724:
	s_add_i32 s8, s0, 8
	s_cmp_gt_i32 s8, s7
	s_cselect_b64 s[2:3], -1, 0
	s_and_b64 vcc, s[2:3], exec
	s_add_i32 s9, s0, 16
	s_cmp_gt_i32 s9, s7
	s_cselect_b32 s0, s0, s9
	s_lshl_b32 s0, s0, 4
	s_ashr_i32 s1, s0, 31
	s_lshl_b64 s[0:1], s[0:1], 7
	s_waitcnt vmcnt(2)
	v_mfma_f32_16x16x32_bf16 v[100:103], v[28:31], v[44:47], 0
	v_mfma_f32_16x16x32_bf16 v[104:107], v[32:35], v[44:47], 0
	v_mfma_f32_16x16x32_bf16 v[108:111], v[24:27], v[44:47], 0
	v_mfma_f32_16x16x32_bf16 v[112:115], v[36:39], v[44:47], 0
	v_mfma_f32_16x16x32_bf16 v[100:103], v[20:23], v[40:43], v[100:103]
	v_mfma_f32_16x16x32_bf16 v[104:107], v[12:15], v[40:43], v[104:107]
	v_mfma_f32_16x16x32_bf16 v[108:111], v[16:19], v[40:43], v[108:111]
	v_mfma_f32_16x16x32_bf16 v[112:115], v[8:11], v[40:43], v[112:115]
	s_nop 4
	v_max_f32_e32 v100, 0, v100
	v_max_f32_e32 v101, 0, v101
	v_max_f32_e32 v102, 0, v102
	v_max_f32_e32 v103, 0, v103
	v_pk_mul_f32 v[116:117], v[64:65], v[100:101]
	v_pk_fma_f32 v[116:117], v[66:67], v[102:103], v[116:117] op_sel:[1,0,0] op_sel_hi:[0,1,1]
	v_add_f32_e32 v116, v116, v117
	v_lshl_add_u64 v[40:41], v[80:81], 0, s[0:1]
	global_load_dwordx4 v[44:47], v[40:41], off
	s_nop 0
	global_load_dwordx4 v[40:43], v[40:41], off offset:1024
	v_max_f32_e32 v104, 0, v104
	v_max_f32_e32 v105, 0, v105
	v_max_f32_e32 v106, 0, v106
	v_max_f32_e32 v107, 0, v107
	v_pk_mul_f32 v[118:119], v[68:69], v[104:105]
	v_pk_fma_f32 v[118:119], v[70:71], v[106:107], v[118:119] op_sel:[1,0,0] op_sel_hi:[0,1,1]
	v_add_f32_e32 v118, v118, v119
	v_max_f32_e32 v108, 0, v108
	v_max_f32_e32 v109, 0, v109
	v_max_f32_e32 v110, 0, v110
	v_max_f32_e32 v111, 0, v111
	v_pk_mul_f32 v[120:121], v[72:73], v[108:109]
	v_pk_fma_f32 v[120:121], v[74:75], v[110:111], v[120:121] op_sel:[1,0,0] op_sel_hi:[0,1,1]
	v_add_f32_e32 v120, v120, v121
	v_max_f32_e32 v112, 0, v112
	v_max_f32_e32 v113, 0, v113
	v_max_f32_e32 v114, 0, v114
	v_max_f32_e32 v115, 0, v115
	v_pk_mul_f32 v[122:123], v[76:77], v[112:113]
	v_pk_fma_f32 v[122:123], v[78:79], v[114:115], v[122:123] op_sel:[1,0,0] op_sel_hi:[0,1,1]
	v_add_f32_e32 v122, v122, v123
	v_cmp_le_i32_e64 s[24:25], v87, v82
	v_cmp_le_i32_e64 s[26:27], v87, v83
	v_permlane16_swap_b32_e32 v116, v118
	v_permlane16_swap_b32_e32 v120, v122
	v_add_f32_e32 v116, v116, v118
	v_add_f32_e32 v120, v120, v122
	v_ashrrev_i32_e32 v124, 31, v116
	v_ashrrev_i32_e32 v126, 31, v120
	v_bitop3_b32 v116, v116, v124, s21 bitop3:0x1e
	v_bitop3_b32 v120, v120, v126, s21 bitop3:0x1e
	v_cndmask_b32_e64 v116, 0, v116, s[24:25]
	v_cndmask_b32_e64 v120, 0, v120, s[26:27]
	ds_write_b32 v133, v116
	ds_write_b32 v134, v120
	v_add_u32_e32 v133, 0x200, v133
	v_add_u32_e32 v134, 0x200, v134
	v_add_u32_e32 v87, 0x80, v87
	s_mov_b32 s0, s8
	s_cbranch_vccnz .Lsc_exit
.Lsc_B:
	s_add_i32 s8, s0, 8
	s_cmp_gt_i32 s8, s7
	s_cselect_b64 s[2:3], -1, 0
	s_and_b64 vcc, s[2:3], exec
	s_add_i32 s9, s0, 16
	s_cmp_gt_i32 s9, s7
	s_cselect_b32 s0, s0, s9
	s_lshl_b32 s0, s0, 4
	s_ashr_i32 s1, s0, 31
	s_lshl_b64 s[0:1], s[0:1], 7
	s_waitcnt vmcnt(2)
	v_mfma_f32_16x16x32_bf16 v[100:103], v[28:31], v[56:59], 0
	v_mfma_f32_16x16x32_bf16 v[104:107], v[32:35], v[56:59], 0
	v_mfma_f32_16x16x32_bf16 v[108:111], v[24:27], v[56:59], 0
	v_mfma_f32_16x16x32_bf16 v[112:115], v[36:39], v[56:59], 0
	v_mfma_f32_16x16x32_bf16 v[100:103], v[20:23], v[60:63], v[100:103]
	v_mfma_f32_16x16x32_bf16 v[104:107], v[12:15], v[60:63], v[104:107]
	v_mfma_f32_16x16x32_bf16 v[108:111], v[16:19], v[60:63], v[108:111]
	v_mfma_f32_16x16x32_bf16 v[112:115], v[8:11], v[60:63], v[112:115]
	s_nop 4
	v_max_f32_e32 v100, 0, v100
	v_max_f32_e32 v101, 0, v101
	v_max_f32_e32 v102, 0, v102
	v_max_f32_e32 v103, 0, v103
	v_pk_mul_f32 v[116:117], v[64:65], v[100:101]
	v_pk_fma_f32 v[116:117], v[66:67], v[102:103], v[116:117] op_sel:[1,0,0] op_sel_hi:[0,1,1]
	v_add_f32_e32 v116, v116, v117
	v_lshl_add_u64 v[60:61], v[80:81], 0, s[0:1]
	global_load_dwordx4 v[56:59], v[60:61], off
	s_nop 0
	global_load_dwordx4 v[60:63], v[60:61], off offset:1024
	v_max_f32_e32 v104, 0, v104
	v_max_f32_e32 v105, 0, v105
	v_max_f32_e32 v106, 0, v106
	v_max_f32_e32 v107, 0, v107
	v_pk_mul_f32 v[118:119], v[68:69], v[104:105]
	v_pk_fma_f32 v[118:119], v[70:71], v[106:107], v[118:119] op_sel:[1,0,0] op_sel_hi:[0,1,1]
	v_add_f32_e32 v118, v118, v119
	v_max_f32_e32 v108, 0, v108
	v_max_f32_e32 v109, 0, v109
	v_max_f32_e32 v110, 0, v110
	v_max_f32_e32 v111, 0, v111
	v_pk_mul_f32 v[120:121], v[72:73], v[108:109]
	v_pk_fma_f32 v[120:121], v[74:75], v[110:111], v[120:121] op_sel:[1,0,0] op_sel_hi:[0,1,1]
	v_add_f32_e32 v120, v120, v121
	v_max_f32_e32 v112, 0, v112
	v_max_f32_e32 v113, 0, v113
	v_max_f32_e32 v114, 0, v114
	v_max_f32_e32 v115, 0, v115
	v_pk_mul_f32 v[122:123], v[76:77], v[112:113]
	v_pk_fma_f32 v[122:123], v[78:79], v[114:115], v[122:123] op_sel:[1,0,0] op_sel_hi:[0,1,1]
	v_add_f32_e32 v122, v122, v123
	v_cmp_le_i32_e64 s[24:25], v87, v82
	v_cmp_le_i32_e64 s[26:27], v87, v83
	v_permlane16_swap_b32_e32 v116, v118
	v_permlane16_swap_b32_e32 v120, v122
	v_add_f32_e32 v116, v116, v118
	v_add_f32_e32 v120, v120, v122
	v_ashrrev_i32_e32 v124, 31, v116
	v_ashrrev_i32_e32 v126, 31, v120
	v_bitop3_b32 v116, v116, v124, s21 bitop3:0x1e
	v_bitop3_b32 v120, v120, v126, s21 bitop3:0x1e
	v_cndmask_b32_e64 v116, 0, v116, s[24:25]
	v_cndmask_b32_e64 v120, 0, v120, s[26:27]
	ds_write_b32 v133, v116
	ds_write_b32 v134, v120
	v_add_u32_e32 v133, 0x200, v133
	v_add_u32_e32 v134, 0x200, v134
	v_add_u32_e32 v87, 0x80, v87
	s_mov_b32 s0, s8
	s_cbranch_vccz .LBB0_724
